# speedup vs baseline: 1.0160x; 1.0090x over previous
_Z11k_chunksortPKiS0_PjS1_PKfS3_S3_S3_S3_PDF16_S4_PfS5_S4_Ph:
	s_cmpk_lt_i32 s2, 0x7d
	s_mov_b64 s[4:5], -1
	s_cbranch_scc0 .LBB0_13
	s_load_dwordx4 s[4:7], s[0:1], 0x0
	s_mul_i32 s3, s2, 0x1400
	v_or_b32_e32 v2, s3, v0
	v_ashrrev_i32_e32 v3, 31, v2
	v_lshlrev_b64 v[4:5], 2, v[2:3]
	s_waitcnt lgkmcnt(0)
	v_lshl_add_u64 v[6:7], s[4:5], 0, v[4:5]
	v_lshl_add_u64 v[4:5], s[6:7], 0, v[4:5]
	global_load_dword v12, v[4:5], off nt
	v_add_u32_e32 v4, 0x400, v2
	v_ashrrev_i32_e32 v5, 31, v4
	global_load_dword v13, v[6:7], off nt
	v_lshlrev_b64 v[6:7], 2, v[4:5]
	v_lshl_add_u64 v[8:9], s[4:5], 0, v[6:7]
	v_lshl_add_u64 v[6:7], s[6:7], 0, v[6:7]
	global_load_dword v14, v[6:7], off nt
	v_add_u32_e32 v6, 0x800, v2
	v_ashrrev_i32_e32 v7, 31, v6
	global_load_dword v15, v[8:9], off nt
	v_lshlrev_b64 v[8:9], 2, v[6:7]
	v_lshl_add_u64 v[10:11], s[4:5], 0, v[8:9]
	v_lshl_add_u64 v[8:9], s[6:7], 0, v[8:9]
	global_load_dword v16, v[8:9], off nt
	v_add_u32_e32 v8, 0xc00, v2
	v_ashrrev_i32_e32 v9, 31, v8
	global_load_dword v17, v[10:11], off nt
	v_lshlrev_b64 v[10:11], 2, v[8:9]
	v_lshl_add_u64 v[18:19], s[4:5], 0, v[10:11]
	v_lshl_add_u64 v[10:11], s[6:7], 0, v[10:11]
	global_load_dword v19, v[18:19], off nt
	s_movk_i32 s3, 0x100
	global_load_dword v18, v[10:11], off nt
	v_add_u32_e32 v10, 0x1000, v2
	v_ashrrev_i32_e32 v11, 31, v10
	v_lshlrev_b64 v[22:23], 2, v[10:11]
	v_lshl_add_u64 v[20:21], s[4:5], 0, v[22:23]
	v_lshl_add_u64 v[22:23], s[6:7], 0, v[22:23]
	global_load_dword v21, v[20:21], off nt
	v_cmp_gt_u32_e32 vcc, s3, v0
	global_load_dword v20, v[22:23], off nt
	v_lshlrev_b32_e32 v1, 2, v0
	s_and_saveexec_b64 s[4:5], vcc
	v_mov_b32_e32 v22, 0
	ds_write_b32 v1, v22 offset:20480
	s_or_b64 exec, exec, s[4:5]
	s_mov_b32 s3, 0x14e5e0b
	s_waitcnt vmcnt(9)
	v_mul_hi_u32 v26, v12, s3
	v_lshlrev_b32_e32 v27, 2, v26
	v_mov_b32_e32 v29, 1
	s_waitcnt vmcnt(7)
	v_mul_hi_u32 v25, v14, s3
	s_waitcnt lgkmcnt(0)
	s_barrier
	ds_add_u32 v27, v29 offset:20480
	v_lshlrev_b32_e32 v28, 2, v25
	s_waitcnt vmcnt(5)
	v_mul_hi_u32 v24, v16, s3
	ds_add_u32 v28, v29 offset:20480
	v_lshlrev_b32_e32 v30, 2, v24
	s_waitcnt vmcnt(2)
	v_mul_hi_u32 v23, v18, s3
	ds_add_u32 v30, v29 offset:20480
	v_lshlrev_b32_e32 v31, 2, v23
	s_waitcnt vmcnt(0)
	v_mul_hi_u32 v22, v20, s3
	ds_add_u32 v31, v29 offset:20480
	v_lshlrev_b32_e32 v32, 2, v22
	ds_add_u32 v32, v29 offset:20480
	v_mov_b32_e32 v29, 0
	s_waitcnt lgkmcnt(0)
	s_barrier
	s_and_saveexec_b64 s[4:5], vcc
	ds_read_b32 v29, v1 offset:20480
	s_or_b64 exec, exec, s[4:5]
	v_mbcnt_lo_u32_b32 v33, -1, 0
	v_mbcnt_hi_u32_b32 v33, -1, v33
	v_and_b32_e32 v34, 64, v33
	v_add_u32_e32 v35, -1, v33
	v_cmp_lt_i32_e64 s[4:5], v35, v34
	v_and_b32_e32 v36, 63, v0
	v_add_u32_e32 v37, -2, v33
	v_cndmask_b32_e64 v35, v35, v33, s[4:5]
	v_lshlrev_b32_e32 v35, 2, v35
	s_waitcnt lgkmcnt(0)
	v_mov_b32_e32 v33, v29
	v_and_b32_e32 v34, 0x33f, v0
	s_nop 1
	v_add_u32_dpp v33, v33, v33 row_shr:1 row_mask:0xf bank_mask:0xf bound_ctrl:0
	s_nop 1
	v_add_u32_dpp v33, v33, v33 row_shr:2 row_mask:0xf bank_mask:0xf bound_ctrl:0
	s_nop 1
	v_add_u32_dpp v33, v33, v33 row_shr:4 row_mask:0xf bank_mask:0xf bound_ctrl:0
	s_nop 1
	v_add_u32_dpp v33, v33, v33 row_shr:8 row_mask:0xf bank_mask:0xf bound_ctrl:0
	s_nop 1
	v_add_u32_dpp v33, v33, v33 row_bcast:15 row_mask:0xa bank_mask:0xf
	s_nop 1
	v_add_u32_dpp v33, v33, v33 row_bcast:31 row_mask:0xc bank_mask:0xf
	v_cmp_eq_u32_e64 s[4:5], 63, v34
	s_and_saveexec_b64 s[6:7], s[4:5]
	v_lshrrev_b32_e32 v34, 4, v0
	v_and_b32_e32 v34, 60, v34
	ds_write_b32 v34, v33 offset:21504
	s_or_b64 exec, exec, s[6:7]
	s_load_dwordx2 s[6:7], s[0:1], 0x18
	s_waitcnt lgkmcnt(0)
	s_barrier
	s_and_saveexec_b64 s[8:9], vcc
	s_cbranch_execz .LBB0_9
	v_mov_b32_e32 v34, 0
	ds_read_b96 v[34:36], v34 offset:21504
	s_movk_i32 s3, 0x7f
	v_cmp_lt_u32_e64 s[4:5], 63, v0
	s_waitcnt lgkmcnt(0)
	s_nop 0
	v_cndmask_b32_e64 v34, 0, v34, s[4:5]
	v_cmp_lt_u32_e64 s[4:5], s3, v0
	s_movk_i32 s3, 0xbf
	v_add_u32_e32 v33, v34, v33
	v_cndmask_b32_e64 v35, 0, v35, s[4:5]
	v_cmp_lt_u32_e64 s[4:5], s3, v0
	s_nop 1
	v_cndmask_b32_e64 v36, 0, v36, s[4:5]
	v_add3_u32 v33, v33, v35, v36

.LBB1_24:
	s_or_b64 exec, exec, s[12:13]
	v_mov_b32_e32 v18, 0
	s_waitcnt lgkmcnt(0)
	s_barrier
	ds_read_b64 v[30:31], v18 offset:22528
	s_and_saveexec_b64 s[10:11], s[8:9]
	v_lshlrev_b32_e32 v18, 2, v0
	ds_read_b32 v18, v18 offset:16384
	s_or_b64 exec, exec, s[10:11]
	v_mbcnt_lo_u32_b32 v19, -1, 0
	v_mbcnt_hi_u32_b32 v21, -1, v19
	v_and_b32_e32 v20, 64, v21
	v_add_u32_e32 v19, -1, v21
	v_cmp_lt_i32_e64 s[10:11], v19, v20
	v_and_b32_e32 v38, 63, v0
	v_add_u32_e32 v39, -2, v21
	v_cndmask_b32_e64 v19, v19, v21, s[10:11]
	v_lshlrev_b32_e32 v19, 2, v19
	s_waitcnt lgkmcnt(0)
	v_mov_b32_e32 v19, v18
	s_nop 1
	v_add_u32_dpp v19, v19, v19 row_shr:1 row_mask:0xf bank_mask:0xf bound_ctrl:0
	s_nop 1
	v_add_u32_dpp v19, v19, v19 row_shr:2 row_mask:0xf bank_mask:0xf bound_ctrl:0
	s_nop 1
	v_add_u32_dpp v19, v19, v19 row_shr:4 row_mask:0xf bank_mask:0xf bound_ctrl:0
	s_nop 1
	v_add_u32_dpp v19, v19, v19 row_shr:8 row_mask:0xf bank_mask:0xf bound_ctrl:0
	s_nop 1
	v_add_u32_dpp v19, v19, v19 row_bcast:15 row_mask:0xa bank_mask:0xf
	s_nop 1
	v_add_u32_dpp v19, v19, v19 row_bcast:31 row_mask:0xc bank_mask:0xf
	v_cmp_gt_u32_e64 s[10:11], 32, v38
	v_and_b32_e32 v39, 0x33f, v0
	v_cmp_eq_u32_e64 s[12:13], 63, v39
	s_and_saveexec_b64 s[14:15], s[12:13]
	v_and_b32_e32 v39, 60, v25
	ds_write_b32 v39, v19 offset:20480
	s_or_b64 exec, exec, s[14:15]
	s_waitcnt lgkmcnt(0)
	s_barrier
	s_and_saveexec_b64 s[18:19], s[8:9]
	s_cbranch_execz .LBB1_31
	v_mov_b32_e32 v39, 0
	ds_read_b96 v[40:42], v39 offset:20480
	s_movk_i32 s14, 0x7f
	v_cmp_lt_u32_e64 s[12:13], 63, v0
	v_sub_u32_e32 v19, v19, v18
	s_waitcnt lgkmcnt(0)
	v_cndmask_b32_e64 v39, 0, v40, s[12:13]
	v_cmp_lt_u32_e64 s[12:13], s14, v0
	v_add_u32_e32 v19, v19, v39
	s_nop 0
	v_cndmask_b32_e64 v40, 0, v41, s[12:13]
	s_movk_i32 s12, 0xbf
	v_cmp_lt_u32_e64 s[12:13], s12, v0
	s_nop 1
	v_cndmask_b32_e64 v41, 0, v42, s[12:13]
	v_add_co_u32_e64 v18, s[12:13], 1, v18
	v_cvt_f32_u32_e32 v18, v18
	v_add3_u32 v19, v19, v40, v41
	v_lshlrev_b32_e32 v40, 2, v0
	v_rsq_f32_e32 v39, v18
	v_add_u32_e32 v18, v19, v30
	ds_write_b32 v40, v18 offset:21504
	v_add_u32_e32 v18, s3, v0
	v_mul_f32_e32 v41, 0x45800000, v39
	s_movk_i32 s3, 0xc4
	v_cndmask_b32_e64 v39, v39, v41, s[12:13]
	v_cmp_gt_u32_e64 s[12:13], s3, v0
	s_mov_b32 s3, 0xc350
	v_cmp_gt_i32_e64 s[14:15], s3, v18
	s_and_b64 s[12:13], s[12:13], s[14:15]
	ds_write2st64_b32 v40, v19, v39 offset0:68 offset1:76
	s_and_b64 exec, exec, s[12:13]
	s_cbranch_execz .LBB1_31
	v_ashrrev_i32_e32 v19, 31, v18
	v_lshl_add_u64 v[18:19], v[18:19], 2, s[30:31]
	global_store_dword v[18:19], v39, off sc0 sc1
